# gemm3 layer-1 residual epilogue software-pipelined too (in-place bf16 stream rows), on top of v24
# speedup vs baseline: 1.0032x; 1.0032x over previous
.LBB0_679:
	s_lshr_b32 s15, s44, 4
	s_cmp_lt_i32 s44, 64
	s_mulk_i32 s15, 0x3000
	s_cselect_b32 s46, s15, 0xc000
	s_lshl_b32 s48, s44, 8
	s_ashr_i32 s49, s48, 31
	s_ashr_i32 s47, s46, 31
	s_lshl_b64 s[48:49], s[48:49], 12
	v_readlane_b32 s4, v252, 45
	v_readlane_b32 s5, v252, 46
	s_add_u32 s48, s4, s48
	s_addc_u32 s49, s5, s49
	s_lshl_b64 s[46:47], s[46:47], 2
	s_add_u32 s46, s53, s46
	v_mov_b32_e32 v7, v5
	v_mov_b32_e32 v6, v175
	s_addc_u32 s47, s55, s47
	s_lshl_b32 s15, s42, 8
	s_or_b32 s15, s15, s56
	v_lshl_add_u32 v236, v175, 2, s15
	v_add_u32_e32 v238, s64, v5
	v_readlane_b32 s4, v255, 43
	v_readlane_b32 s5, v255, 44
	v_lshlrev_b32_e32 v237, 2, v236
	v_lshlrev_b32_e32 v236, 1, v236
	v_lshl_add_u32 v6, v238, 12, v236
	v_add_u32_e32 v7, 0x10000, v6
	v_add_u32_e32 v36, 0x20000, v6
	v_add_u32_e32 v37, 0x30000, v6
	v_add_u32_e32 v172, 0x80000, v6
	v_add_u32_e32 v173, 0x90000, v6
	v_add_u32_e32 v180, 0xa0000, v6
	v_add_u32_e32 v181, 0xb0000, v6
	global_load_dwordx4 v[8:11], v237, s[46:47]
	global_load_dwordx4 v[24:27], v237, s[4:5]
	global_load_dwordx4 v[12:15], v237, s[46:47] offset:64
	global_load_dwordx4 v[28:31], v237, s[4:5] offset:64
	global_load_dwordx4 v[16:19], v237, s[46:47] offset:512
	global_load_dwordx4 v[32:35], v237, s[4:5] offset:512
	global_load_dwordx4 v[20:23], v237, s[46:47] offset:576
	global_load_dwordx4 v[176:179], v237, s[4:5] offset:576
	global_load_dwordx2 v[186:187], v6, s[48:49]
	global_load_dwordx2 v[190:191], v6, s[48:49] offset:32
	global_load_dwordx2 v[216:217], v7, s[48:49]
	global_load_dwordx2 v[220:221], v7, s[48:49] offset:32
	global_load_dwordx2 v[224:225], v36, s[48:49]
	global_load_dwordx2 v[228:229], v36, s[48:49] offset:32
	global_load_dwordx2 v[232:233], v37, s[48:49]
	s_mov_b32 s4, 0x37800000
	v_readlane_b32 s74, v255, 24
	v_readlane_b32 s76, v255, 26
	s_mov_b64 s[42:43], -1
	v_readlane_b32 s75, v255, 25
	v_readlane_b32 s77, v255, 27
	s_waitcnt vmcnt(7)
	v_pk_add_f32 v[8:9], v[8:9], v[24:25]
	v_pk_add_f32 v[10:11], v[10:11], v[26:27]
	v_pk_mul_f32 v[8:9], v[8:9], s[4:5] op_sel_hi:[1,0]
	v_pk_mul_f32 v[10:11], v[10:11], s[4:5] op_sel_hi:[1,0]
	v_pk_add_f32 v[12:13], v[12:13], v[28:29]
	v_pk_add_f32 v[14:15], v[14:15], v[30:31]
	v_pk_mul_f32 v[12:13], v[12:13], s[4:5] op_sel_hi:[1,0]
	v_pk_mul_f32 v[14:15], v[14:15], s[4:5] op_sel_hi:[1,0]
	v_pk_add_f32 v[16:17], v[16:17], v[32:33]
	v_pk_add_f32 v[18:19], v[18:19], v[34:35]
	v_pk_mul_f32 v[16:17], v[16:17], s[4:5] op_sel_hi:[1,0]
	v_pk_mul_f32 v[18:19], v[18:19], s[4:5] op_sel_hi:[1,0]
	v_pk_add_f32 v[20:21], v[20:21], v[176:177]
	v_pk_add_f32 v[22:23], v[22:23], v[178:179]
	v_pk_mul_f32 v[20:21], v[20:21], s[4:5] op_sel_hi:[1,0]
	v_pk_mul_f32 v[22:23], v[22:23], s[4:5] op_sel_hi:[1,0]
	global_load_dwordx2 v[24:25], v37, s[48:49] offset:32
	global_load_dwordx2 v[28:29], v172, s[48:49]
	global_load_dwordx2 v[32:33], v172, s[48:49] offset:32
	global_load_dwordx2 v[176:177], v173, s[48:49]
	s_waitcnt vmcnt(10)
	v_and_b32_e32 v189, 0xffff0000, v187
	v_lshlrev_b32_e32 v188, 16, v187
	v_and_b32_e32 v187, 0xffff0000, v186
	v_lshlrev_b32_e32 v186, 16, v186
	v_pk_fma_f32 v[162:163], v[162:163], v[8:9], v[186:187]
	v_pk_fma_f32 v[164:165], v[164:165], v[10:11], v[188:189]
	v_cvt_pk_bf16_f32 v162, v162, v163
	v_cvt_pk_bf16_f32 v163, v164, v165
	global_store_dwordx2 v6, v[162:163], s[48:49]
	global_load_dwordx2 v[186:187], v173, s[48:49] offset:32
	global_load_dwordx2 v[162:163], v180, s[48:49]
	s_waitcnt vmcnt(12)
	v_and_b32_e32 v193, 0xffff0000, v191
	v_lshlrev_b32_e32 v192, 16, v191
	v_and_b32_e32 v191, 0xffff0000, v190
	v_lshlrev_b32_e32 v190, 16, v190
	v_pk_fma_f32 v[134:135], v[134:135], v[12:13], v[190:191]
	v_pk_fma_f32 v[136:137], v[136:137], v[14:15], v[192:193]
	v_cvt_pk_bf16_f32 v134, v134, v135
	v_cvt_pk_bf16_f32 v135, v136, v137
	global_store_dwordx2 v6, v[134:135], s[48:49] offset:32
	global_load_dwordx2 v[190:191], v180, s[48:49] offset:32
	global_load_dwordx2 v[134:135], v181, s[48:49]
	s_waitcnt vmcnt(14)
	v_and_b32_e32 v219, 0xffff0000, v217
	v_lshlrev_b32_e32 v218, 16, v217
	v_and_b32_e32 v217, 0xffff0000, v216
	v_lshlrev_b32_e32 v216, 16, v216
	v_pk_fma_f32 v[158:159], v[158:159], v[8:9], v[216:217]
	v_pk_fma_f32 v[160:161], v[160:161], v[10:11], v[218:219]
	v_cvt_pk_bf16_f32 v158, v158, v159
	v_cvt_pk_bf16_f32 v159, v160, v161
	global_store_dwordx2 v7, v[158:159], s[48:49]
	global_load_dwordx2 v[216:217], v181, s[48:49] offset:32
	global_load_dwordx2 v[158:159], v6, s[48:49] offset:256
	s_waitcnt vmcnt(16)
	v_and_b32_e32 v223, 0xffff0000, v221
	v_lshlrev_b32_e32 v222, 16, v221
	v_and_b32_e32 v221, 0xffff0000, v220
	v_lshlrev_b32_e32 v220, 16, v220
	v_pk_fma_f32 v[126:127], v[126:127], v[12:13], v[220:221]
	v_pk_fma_f32 v[128:129], v[128:129], v[14:15], v[222:223]
	v_cvt_pk_bf16_f32 v126, v126, v127
	v_cvt_pk_bf16_f32 v127, v128, v129
	global_store_dwordx2 v7, v[126:127], s[48:49] offset:32
	global_load_dwordx2 v[220:221], v6, s[48:49] offset:288
	global_load_dwordx2 v[126:127], v7, s[48:49] offset:256
	s_waitcnt vmcnt(18)
	v_and_b32_e32 v227, 0xffff0000, v225
	v_lshlrev_b32_e32 v226, 16, v225
	v_and_b32_e32 v225, 0xffff0000, v224
	v_lshlrev_b32_e32 v224, 16, v224
	v_pk_fma_f32 v[154:155], v[154:155], v[8:9], v[224:225]
	v_pk_fma_f32 v[156:157], v[156:157], v[10:11], v[226:227]
	v_cvt_pk_bf16_f32 v154, v154, v155
	v_cvt_pk_bf16_f32 v155, v156, v157
	global_store_dwordx2 v36, v[154:155], s[48:49]
	global_load_dwordx2 v[224:225], v7, s[48:49] offset:288
	global_load_dwordx2 v[154:155], v36, s[48:49] offset:256
	s_waitcnt vmcnt(20)
	v_and_b32_e32 v231, 0xffff0000, v229
	v_lshlrev_b32_e32 v230, 16, v229
	v_and_b32_e32 v229, 0xffff0000, v228
	v_lshlrev_b32_e32 v228, 16, v228
	v_pk_fma_f32 v[122:123], v[122:123], v[12:13], v[228:229]
	v_pk_fma_f32 v[124:125], v[124:125], v[14:15], v[230:231]
	v_cvt_pk_bf16_f32 v122, v122, v123
	v_cvt_pk_bf16_f32 v123, v124, v125
	global_store_dwordx2 v36, v[122:123], s[48:49] offset:32
	global_load_dwordx2 v[228:229], v36, s[48:49] offset:288
	global_load_dwordx2 v[122:123], v37, s[48:49] offset:256
	s_waitcnt vmcnt(22)
	v_and_b32_e32 v235, 0xffff0000, v233
	v_lshlrev_b32_e32 v234, 16, v233
	v_and_b32_e32 v233, 0xffff0000, v232
	v_lshlrev_b32_e32 v232, 16, v232
	v_pk_fma_f32 v[150:151], v[150:151], v[8:9], v[232:233]
	v_pk_fma_f32 v[152:153], v[152:153], v[10:11], v[234:235]
	v_cvt_pk_bf16_f32 v150, v150, v151
	v_cvt_pk_bf16_f32 v151, v152, v153
	global_store_dwordx2 v37, v[150:151], s[48:49]
	global_load_dwordx2 v[232:233], v37, s[48:49] offset:288
	global_load_dwordx2 v[150:151], v172, s[48:49] offset:256
	s_waitcnt vmcnt(24)
	v_and_b32_e32 v27, 0xffff0000, v25
	v_lshlrev_b32_e32 v26, 16, v25
	v_and_b32_e32 v25, 0xffff0000, v24
	v_lshlrev_b32_e32 v24, 16, v24
	v_pk_fma_f32 v[118:119], v[118:119], v[12:13], v[24:25]
	v_pk_fma_f32 v[120:121], v[120:121], v[14:15], v[26:27]
	v_cvt_pk_bf16_f32 v118, v118, v119
	v_cvt_pk_bf16_f32 v119, v120, v121
	global_store_dwordx2 v37, v[118:119], s[48:49] offset:32
	global_load_dwordx2 v[24:25], v172, s[48:49] offset:288
	global_load_dwordx2 v[118:119], v173, s[48:49] offset:256
	s_waitcnt vmcnt(26)
	v_and_b32_e32 v31, 0xffff0000, v29
	v_lshlrev_b32_e32 v30, 16, v29
	v_and_b32_e32 v29, 0xffff0000, v28
	v_lshlrev_b32_e32 v28, 16, v28
	v_pk_fma_f32 v[146:147], v[146:147], v[8:9], v[28:29]
	v_pk_fma_f32 v[148:149], v[148:149], v[10:11], v[30:31]
	v_cvt_pk_bf16_f32 v146, v146, v147
	v_cvt_pk_bf16_f32 v147, v148, v149
	global_store_dwordx2 v172, v[146:147], s[48:49]
	global_load_dwordx2 v[28:29], v173, s[48:49] offset:288
	global_load_dwordx2 v[146:147], v180, s[48:49] offset:256
	s_waitcnt vmcnt(28)
	v_and_b32_e32 v35, 0xffff0000, v33
	v_lshlrev_b32_e32 v34, 16, v33
	v_and_b32_e32 v33, 0xffff0000, v32
	v_lshlrev_b32_e32 v32, 16, v32
	v_pk_fma_f32 v[114:115], v[114:115], v[12:13], v[32:33]
	v_pk_fma_f32 v[116:117], v[116:117], v[14:15], v[34:35]
	v_cvt_pk_bf16_f32 v114, v114, v115
	v_cvt_pk_bf16_f32 v115, v116, v117
	global_store_dwordx2 v172, v[114:115], s[48:49] offset:32
	global_load_dwordx2 v[32:33], v180, s[48:49] offset:288
	global_load_dwordx2 v[114:115], v181, s[48:49] offset:256
	s_waitcnt vmcnt(30)
	v_and_b32_e32 v179, 0xffff0000, v177
	v_lshlrev_b32_e32 v178, 16, v177
	v_and_b32_e32 v177, 0xffff0000, v176
	v_lshlrev_b32_e32 v176, 16, v176
	v_pk_fma_f32 v[142:143], v[142:143], v[8:9], v[176:177]
	v_pk_fma_f32 v[144:145], v[144:145], v[10:11], v[178:179]
	v_cvt_pk_bf16_f32 v142, v142, v143
	v_cvt_pk_bf16_f32 v143, v144, v145
	global_store_dwordx2 v173, v[142:143], s[48:49]
	global_load_dwordx2 v[176:177], v181, s[48:49] offset:288
	s_waitcnt vmcnt(30)
	v_and_b32_e32 v189, 0xffff0000, v187
	v_lshlrev_b32_e32 v188, 16, v187
	v_and_b32_e32 v187, 0xffff0000, v186
	v_lshlrev_b32_e32 v186, 16, v186
	v_pk_fma_f32 v[110:111], v[110:111], v[12:13], v[186:187]
	v_pk_fma_f32 v[112:113], v[112:113], v[14:15], v[188:189]
	v_cvt_pk_bf16_f32 v110, v110, v111
	v_cvt_pk_bf16_f32 v111, v112, v113
	global_store_dwordx2 v173, v[110:111], s[48:49] offset:32
	s_waitcnt vmcnt(30)
	v_and_b32_e32 v165, 0xffff0000, v163
	v_lshlrev_b32_e32 v164, 16, v163
	v_and_b32_e32 v163, 0xffff0000, v162
	v_lshlrev_b32_e32 v162, 16, v162
	v_pk_fma_f32 v[138:139], v[138:139], v[8:9], v[162:163]
	v_pk_fma_f32 v[140:141], v[140:141], v[10:11], v[164:165]
	v_cvt_pk_bf16_f32 v138, v138, v139
	v_cvt_pk_bf16_f32 v139, v140, v141
	global_store_dwordx2 v180, v[138:139], s[48:49]
	s_waitcnt vmcnt(29)
	v_and_b32_e32 v193, 0xffff0000, v191
	v_lshlrev_b32_e32 v192, 16, v191
	v_and_b32_e32 v191, 0xffff0000, v190
	v_lshlrev_b32_e32 v190, 16, v190
	v_pk_fma_f32 v[106:107], v[106:107], v[12:13], v[190:191]
	v_pk_fma_f32 v[108:109], v[108:109], v[14:15], v[192:193]
	v_cvt_pk_bf16_f32 v106, v106, v107
	v_cvt_pk_bf16_f32 v107, v108, v109
	global_store_dwordx2 v180, v[106:107], s[48:49] offset:32
	s_waitcnt vmcnt(29)
	v_and_b32_e32 v137, 0xffff0000, v135
	v_lshlrev_b32_e32 v136, 16, v135
	v_and_b32_e32 v135, 0xffff0000, v134
	v_lshlrev_b32_e32 v134, 16, v134
	v_pk_fma_f32 v[130:131], v[130:131], v[8:9], v[134:135]
	v_pk_fma_f32 v[132:133], v[132:133], v[10:11], v[136:137]
	v_cvt_pk_bf16_f32 v130, v130, v131
	v_cvt_pk_bf16_f32 v131, v132, v133
	global_store_dwordx2 v181, v[130:131], s[48:49]
	s_waitcnt vmcnt(28)
	v_and_b32_e32 v219, 0xffff0000, v217
	v_lshlrev_b32_e32 v218, 16, v217
	v_and_b32_e32 v217, 0xffff0000, v216
	v_lshlrev_b32_e32 v216, 16, v216
	v_pk_fma_f32 v[102:103], v[102:103], v[12:13], v[216:217]
	v_pk_fma_f32 v[104:105], v[104:105], v[14:15], v[218:219]
	v_cvt_pk_bf16_f32 v102, v102, v103
	v_cvt_pk_bf16_f32 v103, v104, v105
	global_store_dwordx2 v181, v[102:103], s[48:49] offset:32
	s_waitcnt vmcnt(28)
	v_and_b32_e32 v161, 0xffff0000, v159
	v_lshlrev_b32_e32 v160, 16, v159
	v_and_b32_e32 v159, 0xffff0000, v158
	v_lshlrev_b32_e32 v158, 16, v158
	v_pk_fma_f32 v[98:99], v[98:99], v[16:17], v[158:159]
	v_pk_fma_f32 v[100:101], v[100:101], v[18:19], v[160:161]
	v_cvt_pk_bf16_f32 v98, v98, v99
	v_cvt_pk_bf16_f32 v99, v100, v101
	global_store_dwordx2 v6, v[98:99], s[48:49] offset:256
	s_waitcnt vmcnt(27)
	v_and_b32_e32 v223, 0xffff0000, v221
	v_lshlrev_b32_e32 v222, 16, v221
	v_and_b32_e32 v221, 0xffff0000, v220
	v_lshlrev_b32_e32 v220, 16, v220
	v_pk_fma_f32 v[70:71], v[70:71], v[20:21], v[220:221]
	v_pk_fma_f32 v[72:73], v[72:73], v[22:23], v[222:223]
	v_cvt_pk_bf16_f32 v70, v70, v71
	v_cvt_pk_bf16_f32 v71, v72, v73
	global_store_dwordx2 v6, v[70:71], s[48:49] offset:288
	s_waitcnt vmcnt(27)
	v_and_b32_e32 v129, 0xffff0000, v127
	v_lshlrev_b32_e32 v128, 16, v127
	v_and_b32_e32 v127, 0xffff0000, v126
	v_lshlrev_b32_e32 v126, 16, v126
	v_pk_fma_f32 v[94:95], v[94:95], v[16:17], v[126:127]
	v_pk_fma_f32 v[96:97], v[96:97], v[18:19], v[128:129]
	v_cvt_pk_bf16_f32 v94, v94, v95
	v_cvt_pk_bf16_f32 v95, v96, v97
	global_store_dwordx2 v7, v[94:95], s[48:49] offset:256
	s_waitcnt vmcnt(26)
	v_and_b32_e32 v227, 0xffff0000, v225
	v_lshlrev_b32_e32 v226, 16, v225
	v_and_b32_e32 v225, 0xffff0000, v224
	v_lshlrev_b32_e32 v224, 16, v224
	v_pk_fma_f32 v[62:63], v[62:63], v[20:21], v[224:225]
	v_pk_fma_f32 v[64:65], v[64:65], v[22:23], v[226:227]
	v_cvt_pk_bf16_f32 v62, v62, v63
	v_cvt_pk_bf16_f32 v63, v64, v65
	global_store_dwordx2 v7, v[62:63], s[48:49] offset:288
	s_waitcnt vmcnt(26)
	v_and_b32_e32 v157, 0xffff0000, v155
	v_lshlrev_b32_e32 v156, 16, v155
	v_and_b32_e32 v155, 0xffff0000, v154
	v_lshlrev_b32_e32 v154, 16, v154
	v_pk_fma_f32 v[90:91], v[90:91], v[16:17], v[154:155]
	v_pk_fma_f32 v[92:93], v[92:93], v[18:19], v[156:157]
	v_cvt_pk_bf16_f32 v90, v90, v91
	v_cvt_pk_bf16_f32 v91, v92, v93
	global_store_dwordx2 v36, v[90:91], s[48:49] offset:256
	s_waitcnt vmcnt(25)
	v_and_b32_e32 v231, 0xffff0000, v229
	v_lshlrev_b32_e32 v230, 16, v229
	v_and_b32_e32 v229, 0xffff0000, v228
	v_lshlrev_b32_e32 v228, 16, v228
	v_pk_fma_f32 v[58:59], v[58:59], v[20:21], v[228:229]
	v_pk_fma_f32 v[60:61], v[60:61], v[22:23], v[230:231]
	v_cvt_pk_bf16_f32 v58, v58, v59
	v_cvt_pk_bf16_f32 v59, v60, v61
	global_store_dwordx2 v36, v[58:59], s[48:49] offset:288
	s_waitcnt vmcnt(25)
	v_and_b32_e32 v125, 0xffff0000, v123
	v_lshlrev_b32_e32 v124, 16, v123
	v_and_b32_e32 v123, 0xffff0000, v122
	v_lshlrev_b32_e32 v122, 16, v122
	v_pk_fma_f32 v[86:87], v[86:87], v[16:17], v[122:123]
	v_pk_fma_f32 v[88:89], v[88:89], v[18:19], v[124:125]
	v_cvt_pk_bf16_f32 v86, v86, v87
	v_cvt_pk_bf16_f32 v87, v88, v89
	global_store_dwordx2 v37, v[86:87], s[48:49] offset:256
	s_waitcnt vmcnt(24)
	v_and_b32_e32 v235, 0xffff0000, v233
	v_lshlrev_b32_e32 v234, 16, v233
	v_and_b32_e32 v233, 0xffff0000, v232
	v_lshlrev_b32_e32 v232, 16, v232
	v_pk_fma_f32 v[54:55], v[54:55], v[20:21], v[232:233]
	v_pk_fma_f32 v[56:57], v[56:57], v[22:23], v[234:235]
	v_cvt_pk_bf16_f32 v54, v54, v55
	v_cvt_pk_bf16_f32 v55, v56, v57
	global_store_dwordx2 v37, v[54:55], s[48:49] offset:288
	s_waitcnt vmcnt(24)
	v_and_b32_e32 v153, 0xffff0000, v151
	v_lshlrev_b32_e32 v152, 16, v151
	v_and_b32_e32 v151, 0xffff0000, v150
	v_lshlrev_b32_e32 v150, 16, v150
	v_pk_fma_f32 v[82:83], v[82:83], v[16:17], v[150:151]
	v_pk_fma_f32 v[84:85], v[84:85], v[18:19], v[152:153]
	v_cvt_pk_bf16_f32 v82, v82, v83
	v_cvt_pk_bf16_f32 v83, v84, v85
	global_store_dwordx2 v172, v[82:83], s[48:49] offset:256
	s_waitcnt vmcnt(23)
	v_and_b32_e32 v27, 0xffff0000, v25
	v_lshlrev_b32_e32 v26, 16, v25
	v_and_b32_e32 v25, 0xffff0000, v24
	v_lshlrev_b32_e32 v24, 16, v24
	v_pk_fma_f32 v[50:51], v[50:51], v[20:21], v[24:25]
	v_pk_fma_f32 v[52:53], v[52:53], v[22:23], v[26:27]
	v_cvt_pk_bf16_f32 v50, v50, v51
	v_cvt_pk_bf16_f32 v51, v52, v53
	global_store_dwordx2 v172, v[50:51], s[48:49] offset:288
	s_waitcnt vmcnt(23)
	v_and_b32_e32 v121, 0xffff0000, v119
	v_lshlrev_b32_e32 v120, 16, v119
	v_and_b32_e32 v119, 0xffff0000, v118
	v_lshlrev_b32_e32 v118, 16, v118
	v_pk_fma_f32 v[78:79], v[78:79], v[16:17], v[118:119]
	v_pk_fma_f32 v[80:81], v[80:81], v[18:19], v[120:121]
	v_cvt_pk_bf16_f32 v78, v78, v79
	v_cvt_pk_bf16_f32 v79, v80, v81
	global_store_dwordx2 v173, v[78:79], s[48:49] offset:256
	s_waitcnt vmcnt(22)
	v_and_b32_e32 v31, 0xffff0000, v29
	v_lshlrev_b32_e32 v30, 16, v29
	v_and_b32_e32 v29, 0xffff0000, v28
	v_lshlrev_b32_e32 v28, 16, v28
	v_pk_fma_f32 v[46:47], v[46:47], v[20:21], v[28:29]
	v_pk_fma_f32 v[48:49], v[48:49], v[22:23], v[30:31]
	v_cvt_pk_bf16_f32 v46, v46, v47
	v_cvt_pk_bf16_f32 v47, v48, v49
	global_store_dwordx2 v173, v[46:47], s[48:49] offset:288
	s_waitcnt vmcnt(22)
	v_and_b32_e32 v149, 0xffff0000, v147
	v_lshlrev_b32_e32 v148, 16, v147
	v_and_b32_e32 v147, 0xffff0000, v146
	v_lshlrev_b32_e32 v146, 16, v146
	v_pk_fma_f32 v[74:75], v[74:75], v[16:17], v[146:147]
	v_pk_fma_f32 v[76:77], v[76:77], v[18:19], v[148:149]
	v_cvt_pk_bf16_f32 v74, v74, v75
	v_cvt_pk_bf16_f32 v75, v76, v77
	global_store_dwordx2 v180, v[74:75], s[48:49] offset:256
	s_waitcnt vmcnt(21)
	v_and_b32_e32 v35, 0xffff0000, v33
	v_lshlrev_b32_e32 v34, 16, v33
	v_and_b32_e32 v33, 0xffff0000, v32
	v_lshlrev_b32_e32 v32, 16, v32
	v_pk_fma_f32 v[42:43], v[42:43], v[20:21], v[32:33]
	v_pk_fma_f32 v[44:45], v[44:45], v[22:23], v[34:35]
	v_cvt_pk_bf16_f32 v42, v42, v43
	v_cvt_pk_bf16_f32 v43, v44, v45
	global_store_dwordx2 v180, v[42:43], s[48:49] offset:288
	s_waitcnt vmcnt(21)
	v_and_b32_e32 v117, 0xffff0000, v115
	v_lshlrev_b32_e32 v116, 16, v115
	v_and_b32_e32 v115, 0xffff0000, v114
	v_lshlrev_b32_e32 v114, 16, v114
	v_pk_fma_f32 v[66:67], v[66:67], v[16:17], v[114:115]
	v_pk_fma_f32 v[68:69], v[68:69], v[18:19], v[116:117]
	v_cvt_pk_bf16_f32 v66, v66, v67
	v_cvt_pk_bf16_f32 v67, v68, v69
	global_store_dwordx2 v181, v[66:67], s[48:49] offset:256
	s_waitcnt vmcnt(20)
	v_and_b32_e32 v179, 0xffff0000, v177
	v_lshlrev_b32_e32 v178, 16, v177
	v_and_b32_e32 v177, 0xffff0000, v176
	v_lshlrev_b32_e32 v176, 16, v176
	v_pk_fma_f32 v[38:39], v[38:39], v[20:21], v[176:177]
	v_pk_fma_f32 v[40:41], v[40:41], v[22:23], v[178:179]
	v_cvt_pk_bf16_f32 v38, v38, v39
	v_cvt_pk_bf16_f32 v39, v40, v41
	global_store_dwordx2 v181, v[38:39], s[48:49] offset:288
	s_andn2_b64 vcc, exec, s[18:19]
	s_cbranch_vccnz .LBB0_670
	s_andn2_b64 vcc, exec, s[10:11]
	s_cbranch_vccnz .LBB0_669
	s_barrier
	s_branch .LBB0_669
